# combine phase: rows double-buffered (next row loads issued before the current row's stores, counted vmcnt)
# speedup vs baseline: 1.0006x; 1.0006x over previous
; #define GAS __attribute__((address_space(1)))
; __device__ __forceinline__ unsigned pk2(float lo, float hi) { unsigned r; asm volatile("v_cvt_pk_bf16_f32 %0, %1, %2" : "=v"(r) : "v"(lo), "v"(hi)); return r; }
; template <bool FINAL, bool ADDY = true>
; __device__ __forceinline__ void combine_phase(Frame& F, float* ssq_out) {
;     const int gw = F.vcu * NWAVES + F.wave, NGW = F.G * NWAVES;
;     bf16* HB = (bf16*)(F.ws + WS_HB); const unsigned char* Y0 = (const unsigned char*)(F.ws + SC_Y); const unsigned char* Y1 = Y0 + (size_t)T * DM;
;     for (int m = gw; m < T; m += NGW) {
;         const GAS u32x4* h4 = (const GAS u32x4*)(HB + (size_t)m * DM) + F.lane; const GAS u32x2* a4 = (const GAS u32x2*)(Y0 + (size_t)m * DM) + F.lane; const GAS u32x2* b4 = (const GAS u32x2*)(Y1 + (size_t)m * DM) + F.lane;
;         float v[4][8]; float s = 0.f;
; #pragma unroll
;         for (int j = 0; j < 4; ++j) { const u32x4 h = h4[64 * j]; u32x2 a = {0u, 0u}, b = {0u, 0u}; if (ADDY) { a = a4[64 * j]; b = b4[64 * j]; }
; #pragma unroll
;             for (int q = 0; q < 4; ++q) { const unsigned aw = q < 2 ? a.x : a.y, bw = q < 2 ? b.x : b.y;
;                 const f32x2 ya = (q & 1) ? __builtin_amdgcn_cvt_pk_f32_fp8((int)aw, true) : __builtin_amdgcn_cvt_pk_f32_fp8((int)aw, false), yb = (q & 1) ? __builtin_amdgcn_cvt_pk_f32_fp8((int)bw, true) : __builtin_amdgcn_cvt_pk_f32_fp8((int)bw, false);
;                 v[j][2 * q] = bf_lo(h[q]) + (ADDY ? (ya.x + yb.x) * (1.f / WD_SCALE) : 0.f); v[j][2 * q + 1] = bf_hi(h[q]) + (ADDY ? (ya.y + yb.y) * (1.f / WD_SCALE) : 0.f); } }
;         if constexpr (!FINAL) {
; #pragma unroll
;             for (int j = 0; j < 4; ++j) { u32x4 w;
; #pragma unroll
;                 for (int q = 0; q < 4; ++q) { w[q] = pk2(v[j][2 * q], v[j][2 * q + 1]); const float lo = bf_lo(w[q]), hi = bf_hi(w[q]); s += lo * lo + hi * hi; }
;                 ((GAS u32x4*)(HB + (size_t)m * DM) + F.lane)[64 * j] = w;
;                 u32x2 w8; w8.x = pk4_fp8(bf_lo(w.x), bf_hi(w.x), bf_lo(w.y), bf_hi(w.y)); w8.y = pk4_fp8(bf_lo(w.z), bf_hi(w.z), bf_lo(w.w), bf_hi(w.w));
;                 ((GAS u32x2*)(F.ws + WS_HB8 + (size_t)m * DM) + F.lane)[64 * j] = w8; }
;             s = wave_sum(s); if (F.lane == 0) ssq_out[m] = s;
.LBB0_881:
	s_cmp_lt_i32 s92, 8
	s_cselect_b64 s[4:5], -1, 0
	s_and_b64 s[4:5], s[4:5], s[2:3]
	s_andn2_b64 vcc, exec, s[4:5]
	s_cbranch_vccnz .LBB0_887
	s_lshl_b32 s2, s77, 3
	s_add_i32 s6, s2, s96
	s_cmpk_gt_i32 s6, 0x7fff
	s_cbranch_scc1 .LBB0_887
	s_ashr_i32 s7, s6, 31
	s_lshl_b32 s8, s33, 3
	s_waitcnt lgkmcnt(0)
	s_lshl_b64 s[10:11], s[6:7], 2
	s_add_u32 s18, s10, 0x220000
	s_waitcnt vmcnt(0)
	v_ashrrev_i32_e32 v1, 31, v0
	s_addc_u32 s19, s11, 0
	s_ashr_i32 s9, s8, 31
	s_lshl_b64 s[12:13], s[6:7], 11
	s_lshl_b64 s[14:15], s[6:7], 12
	v_cmp_eq_u32_e64 s[2:3], 0, v0
	s_lshl_b64 s[10:11], s[8:9], 2
	v_lshl_add_u64 v[2:3], v[0:1], 3, s[12:13]
	s_lshl_b64 s[12:13], s[8:9], 11
	v_lshl_add_u64 v[0:1], v[0:1], 4, s[14:15]
	s_lshl_b64 s[14:15], s[8:9], 12
	v_mov_b32_e32 v8, 0
	s_mov_b32 s7, 0xa000000
	v_lshl_add_u64 v[4:5], s[28:29], 0, v[0:1]
	v_lshl_add_u64 v[26:27], s[28:29], 0, v[2:3]
	v_add_co_u32_e32 v4, vcc, 0x12000000, v4
	s_nop 1
	v_addc_co_u32_e32 v5, vcc, 0, v5, vcc
	v_add_co_u32_e32 v32, vcc, 0x1e800000, v26
	s_nop 1
	v_addc_co_u32_e32 v33, vcc, 0, v27, vcc
	global_load_dwordx4 v[10:13], v[4:5], off
	global_load_dwordx4 v[14:17], v[4:5], off offset:1024
	global_load_dwordx4 v[18:21], v[4:5], off offset:2048
	global_load_dwordx4 v[22:25], v[4:5], off offset:3072
	global_load_dwordx2 v[28:29], v[32:33], off
	global_load_dwordx2 v[30:31], v[32:33], off offset:512
	global_load_dwordx2 v[34:35], v[32:33], off offset:1024
	global_load_dwordx2 v[42:43], v[32:33], off offset:1536
	v_add_co_u32_e32 v32, vcc, 0x22800000, v26
	s_nop 1
	v_addc_co_u32_e32 v33, vcc, 0, v27, vcc
	global_load_dwordx2 v[36:37], v[32:33], off
	global_load_dwordx2 v[38:39], v[32:33], off offset:512
	global_load_dwordx2 v[40:41], v[32:33], off offset:1024
	global_load_dwordx2 v[44:45], v[32:33], off offset:1536
	v_add_co_u32_e32 v6, vcc, s7, v26
	s_nop 1
	v_addc_co_u32_e32 v7, vcc, 0, v27, vcc
	s_mov_b64 s[98:99], s[18:19]
	s_add_i32 s6, s6, s8
	s_cmp_lt_i32 s6, 0x8000
	s_cbranch_scc0 .Lp7_noadv_A0
	s_add_u32 s18, s18, s10
	s_addc_u32 s19, s19, s11
	v_lshl_add_u64 v[2:3], v[2:3], 0, s[12:13]
	v_lshl_add_u64 v[0:1], v[0:1], 0, s[14:15]
.Lp7_noadv_A0:
	v_lshl_add_u64 v[116:117], s[28:29], 0, v[0:1]
	v_lshl_add_u64 v[26:27], s[28:29], 0, v[2:3]
	v_add_co_u32_e32 v116, vcc, 0x12000000, v116
	s_nop 1
	v_addc_co_u32_e32 v117, vcc, 0, v117, vcc
	v_add_co_u32_e32 v32, vcc, 0x1e800000, v26
	s_nop 1
	v_addc_co_u32_e32 v33, vcc, 0, v27, vcc
	global_load_dwordx4 v[120:123], v[116:117], off
	global_load_dwordx4 v[124:127], v[116:117], off offset:1024
	global_load_dwordx4 v[128:131], v[116:117], off offset:2048
	global_load_dwordx4 v[132:135], v[116:117], off offset:3072
	global_load_dwordx2 v[136:137], v[32:33], off
	global_load_dwordx2 v[138:139], v[32:33], off offset:512
	global_load_dwordx2 v[140:141], v[32:33], off offset:1024
	global_load_dwordx2 v[148:149], v[32:33], off offset:1536
	v_add_co_u32_e32 v32, vcc, 0x22800000, v26
	s_nop 1
	v_addc_co_u32_e32 v33, vcc, 0, v27, vcc
	global_load_dwordx2 v[142:143], v[32:33], off
	global_load_dwordx2 v[144:145], v[32:33], off offset:512
	global_load_dwordx2 v[146:147], v[32:33], off offset:1024
	global_load_dwordx2 v[150:151], v[32:33], off offset:1536
	v_add_co_u32_e32 v118, vcc, s7, v26
	s_nop 1
	v_addc_co_u32_e32 v119, vcc, 0, v27, vcc
	s_mov_b64 s[100:101], s[18:19]
	s_add_i32 s6, s6, s8
	s_cmp_lt_i32 s6, 0x8000
	s_cbranch_scc0 .Lp7_noadv_B0
	s_add_u32 s18, s18, s10
	s_addc_u32 s19, s19, s11
	v_lshl_add_u64 v[2:3], v[2:3], 0, s[12:13]
	v_lshl_add_u64 v[0:1], v[0:1], 0, s[14:15]
.Lp7_noadv_B0:
	s_waitcnt vmcnt(12)
	s_branch .Lp7_compA

; #define GAS __attribute__((address_space(1)))
; __device__ __forceinline__ unsigned pk2(float lo, float hi) { unsigned r; asm volatile("v_cvt_pk_bf16_f32 %0, %1, %2" : "=v"(r) : "v"(lo), "v"(hi)); return r; }
; __device__ __forceinline__ unsigned pk4_fp8(float a, float b, float c, float d) { unsigned w = 0u; w = __builtin_amdgcn_cvt_pk_fp8_f32(a, b, w, false); w = __builtin_amdgcn_cvt_pk_fp8_f32(c, d, w, true); return w; }
; template <bool FINAL, bool ADDY = true>
; __device__ __forceinline__ void combine_phase(Frame& F, float* ssq_out) {
;     ...
;         const GAS u32x4* h4 = (const GAS u32x4*)(HB + (size_t)m * DM) + F.lane; const GAS u32x2* a4 = (const GAS u32x2*)(Y0 + (size_t)m * DM) + F.lane; const GAS u32x2* b4 = (const GAS u32x2*)(Y1 + (size_t)m * DM) + F.lane;
;         float v[4][8]; float s = 0.f;
; #pragma unroll
;         for (int j = 0; j < 4; ++j) { const u32x4 h = h4[64 * j]; u32x2 a = {0u, 0u}, b = {0u, 0u}; if (ADDY) { a = a4[64 * j]; b = b4[64 * j]; }
; #pragma unroll
;             for (int q = 0; q < 4; ++q) { const unsigned aw = q < 2 ? a.x : a.y, bw = q < 2 ? b.x : b.y;
;                 const f32x2 ya = (q & 1) ? __builtin_amdgcn_cvt_pk_f32_fp8((int)aw, true) : __builtin_amdgcn_cvt_pk_f32_fp8((int)aw, false), yb = (q & 1) ? __builtin_amdgcn_cvt_pk_f32_fp8((int)bw, true) : __builtin_amdgcn_cvt_pk_f32_fp8((int)bw, false);
;                 v[j][2 * q] = bf_lo(h[q]) + (ADDY ? (ya.x + yb.x) * (1.f / WD_SCALE) : 0.f); v[j][2 * q + 1] = bf_hi(h[q]) + (ADDY ? (ya.y + yb.y) * (1.f / WD_SCALE) : 0.f); } }
;         if constexpr (!FINAL) {
; #pragma unroll
;             for (int j = 0; j < 4; ++j) { u32x4 w;
; #pragma unroll
;                 for (int q = 0; q < 4; ++q) { w[q] = pk2(v[j][2 * q], v[j][2 * q + 1]); const float lo = bf_lo(w[q]), hi = bf_hi(w[q]); s += lo * lo + hi * hi; }
;                 ((GAS u32x4*)(HB + (size_t)m * DM) + F.lane)[64 * j] = w;
;                 u32x2 w8; w8.x = pk4_fp8(bf_lo(w.x), bf_hi(w.x), bf_lo(w.y), bf_hi(w.y)); w8.y = pk4_fp8(bf_lo(w.z), bf_hi(w.z), bf_lo(w.w), bf_hi(w.w));
;                 ((GAS u32x2*)(F.ws + WS_HB8 + (size_t)m * DM) + F.lane)[64 * j] = w8; }
.Lp7_noadv_B1:
	s_waitcnt vmcnt(21)
.Lp7_compA:
	v_lshlrev_b32_e32 v9, 16, v10
	v_and_b32_e32 v64, 0xffff0000, v10
	v_lshlrev_b32_e32 v65, 16, v11
	v_and_b32_e32 v66, 0xffff0000, v11
	v_cvt_pk_f32_fp8_e32 v[10:11], v28
	v_cvt_pk_f32_fp8_e32 v[50:51], v36
	v_lshlrev_b32_e32 v67, 16, v12
	v_and_b32_e32 v68, 0xffff0000, v12
	v_lshlrev_b32_e32 v69, 16, v13
	v_and_b32_e32 v70, 0xffff0000, v13
	v_lshlrev_b32_e32 v71, 16, v14
	v_and_b32_e32 v72, 0xffff0000, v14
	v_lshlrev_b32_e32 v73, 16, v15
	v_and_b32_e32 v74, 0xffff0000, v15
	v_cvt_pk_f32_fp8_sdwa v[12:13], v28 src0_sel:WORD_1
	v_cvt_pk_f32_fp8_e32 v[14:15], v29
	v_cvt_pk_f32_fp8_sdwa v[52:53], v36 src0_sel:WORD_1
	v_cvt_pk_f32_fp8_e32 v[54:55], v37
	v_lshlrev_b32_e32 v75, 16, v16
	v_and_b32_e32 v76, 0xffff0000, v16
	v_lshlrev_b32_e32 v77, 16, v17
	v_and_b32_e32 v78, 0xffff0000, v17
	v_cvt_pk_f32_fp8_sdwa v[16:17], v29 src0_sel:WORD_1
	v_cvt_pk_f32_fp8_sdwa v[36:37], v37 src0_sel:WORD_1
	v_pk_add_f32 v[10:11], v[10:11], v[50:51]
	v_cvt_pk_f32_fp8_sdwa v[48:49], v34 src0_sel:WORD_1
	v_pk_add_f32 v[12:13], v[12:13], v[52:53]
	v_pk_add_f32 v[14:15], v[14:15], v[54:55]
	v_fmac_f32_e32 v9, 0x3d800000, v10
	v_fmac_f32_e32 v64, 0x3d800000, v11
	v_cvt_pk_f32_fp8_sdwa v[10:11], v40 src0_sel:WORD_1
	v_fmac_f32_e32 v65, 0x3d800000, v12
	v_fmac_f32_e32 v66, 0x3d800000, v13
	v_fmac_f32_e32 v67, 0x3d800000, v14
	v_fmac_f32_e32 v68, 0x3d800000, v15
	v_cvt_pk_f32_fp8_e32 v[12:13], v35
	v_cvt_pk_f32_fp8_e32 v[14:15], v41
	v_pk_add_f32 v[16:17], v[16:17], v[36:37]
	v_lshlrev_b32_e32 v79, 16, v18
	v_fmac_f32_e32 v69, 0x3d800000, v16
	v_fmac_f32_e32 v70, 0x3d800000, v17
	v_and_b32_e32 v16, 0xffff0000, v18
	v_lshlrev_b32_e32 v17, 16, v19
	v_pk_add_f32 v[10:11], v[48:49], v[10:11]
	v_and_b32_e32 v18, 0xffff0000, v19
	v_fmac_f32_e32 v17, 0x3d800000, v10
	v_fmac_f32_e32 v18, 0x3d800000, v11
	v_pk_add_f32 v[10:11], v[12:13], v[14:15]
	v_cvt_pk_f32_fp8_sdwa v[12:13], v35 src0_sel:WORD_1
	v_cvt_pk_f32_fp8_sdwa v[14:15], v41 src0_sel:WORD_1
	v_cvt_pk_f32_fp8_e32 v[26:27], v30
	v_cvt_pk_f32_fp8_e32 v[56:57], v38
	v_lshlrev_b32_e32 v19, 16, v20
	v_and_b32_e32 v20, 0xffff0000, v20
	v_fmac_f32_e32 v19, 0x3d800000, v10
	v_fmac_f32_e32 v20, 0x3d800000, v11
	v_pk_add_f32 v[10:11], v[12:13], v[14:15]
	v_cvt_pk_f32_fp8_e32 v[12:13], v42
	v_cvt_pk_f32_fp8_e32 v[14:15], v44
	v_pk_add_f32 v[26:27], v[26:27], v[56:57]
	v_cvt_pk_f32_fp8_sdwa v[28:29], v30 src0_sel:WORD_1
	v_fmac_f32_e32 v71, 0x3d800000, v26
	v_lshlrev_b32_e32 v26, 16, v21
	v_and_b32_e32 v21, 0xffff0000, v21
	v_fmac_f32_e32 v26, 0x3d800000, v10
	v_fmac_f32_e32 v21, 0x3d800000, v11
	v_pk_add_f32 v[10:11], v[12:13], v[14:15]
	v_cvt_pk_f32_fp8_sdwa v[12:13], v42 src0_sel:WORD_1
	v_cvt_pk_f32_fp8_sdwa v[14:15], v44 src0_sel:WORD_1
	v_cvt_pk_f32_fp8_sdwa v[58:59], v38 src0_sel:WORD_1
	v_fmac_f32_e32 v72, 0x3d800000, v27
	v_lshlrev_b32_e32 v27, 16, v22
	v_and_b32_e32 v22, 0xffff0000, v22
	v_fmac_f32_e32 v27, 0x3d800000, v10
	v_fmac_f32_e32 v22, 0x3d800000, v11
	v_pk_add_f32 v[10:11], v[12:13], v[14:15]
	v_cvt_pk_f32_fp8_e32 v[12:13], v43
	v_cvt_pk_f32_fp8_e32 v[14:15], v45
	v_pk_add_f32 v[28:29], v[28:29], v[58:59]
	v_cvt_pk_f32_fp8_e32 v[32:33], v31
	v_cvt_pk_f32_fp8_sdwa v[30:31], v31 src0_sel:WORD_1
	v_cvt_pk_f32_fp8_e32 v[60:61], v39
	v_cvt_pk_f32_fp8_sdwa v[38:39], v39 src0_sel:WORD_1
	v_fmac_f32_e32 v73, 0x3d800000, v28
	v_lshlrev_b32_e32 v28, 16, v23
	v_and_b32_e32 v23, 0xffff0000, v23
	v_fmac_f32_e32 v28, 0x3d800000, v10
	v_fmac_f32_e32 v23, 0x3d800000, v11
	v_pk_add_f32 v[10:11], v[12:13], v[14:15]
	v_cvt_pk_f32_fp8_sdwa v[12:13], v43 src0_sel:WORD_1
	v_cvt_pk_f32_fp8_sdwa v[14:15], v45 src0_sel:WORD_1
	v_pk_add_f32 v[30:31], v[30:31], v[38:39]
	v_fmac_f32_e32 v74, 0x3d800000, v29
	v_lshlrev_b32_e32 v29, 16, v24
	v_and_b32_e32 v24, 0xffff0000, v24
	v_pk_add_f32 v[32:33], v[32:33], v[60:61]
	v_fmac_f32_e32 v77, 0x3d800000, v30
	v_fmac_f32_e32 v29, 0x3d800000, v10
	v_fmac_f32_e32 v24, 0x3d800000, v11
	v_lshlrev_b32_e32 v30, 16, v25
	v_pk_add_f32 v[10:11], v[12:13], v[14:15]
	v_and_b32_e32 v25, 0xffff0000, v25
	v_fmac_f32_e32 v75, 0x3d800000, v32
	v_fmac_f32_e32 v30, 0x3d800000, v10
	v_fmac_f32_e32 v25, 0x3d800000, v11
	v_cvt_pk_bf16_f32 v10, v9, v64
	v_cvt_pk_bf16_f32 v11, v65, v66
	v_fmac_f32_e32 v78, 0x3d800000, v31
	v_and_b32_e32 v15, 0xffff0000, v10
	v_and_b32_e32 v32, 0xffff0000, v11
	v_lshlrev_b32_e32 v9, 16, v10
	v_mul_f32_e32 v12, v15, v15
	v_lshlrev_b32_e32 v31, 16, v11
	v_mul_f32_e32 v13, v32, v32
	v_fmac_f32_e32 v12, v9, v9
	v_fmac_f32_e32 v13, v31, v31
	v_cvt_pk_f32_fp8_e32 v[46:47], v34
	v_add_f32_e32 v13, v12, v13
	v_cvt_pk_bf16_f32 v12, v67, v68
	v_fmac_f32_e32 v76, 0x3d800000, v33
	v_and_b32_e32 v34, 0xffff0000, v12
	v_lshlrev_b32_e32 v33, 16, v12
	v_mul_f32_e32 v14, v34, v34
	v_fmac_f32_e32 v14, v33, v33
	v_cvt_pk_f32_fp8_e32 v[62:63], v40
	v_add_f32_e32 v35, v13, v14
	v_mov_b32_e32 v14, 0
	v_cvt_pk_fp8_f32 v14, v9, v15
	v_mov_b32_e32 v15, 0
	v_cvt_pk_fp8_f32 v15, v33, v34
	v_pk_add_f32 v[36:37], v[46:47], v[62:63]
	v_cvt_pk_bf16_f32 v13, v69, v70
	v_cvt_pk_fp8_f32 v14, v31, v32 op_sel:[0,0,1]
	v_fmac_f32_e32 v79, 0x3d800000, v36
	v_fmac_f32_e32 v16, 0x3d800000, v37
	v_lshlrev_b32_e32 v36, 16, v13
	v_and_b32_e32 v37, 0xffff0000, v13
	v_cvt_pk_fp8_f32 v15, v36, v37 op_sel:[0,0,1]
	v_mul_f32_e32 v38, v37, v37
	global_store_dwordx4 v[4:5], v[10:13], off
	global_store_dwordx2 v[6:7], v[14:15], off
	v_fmac_f32_e32 v38, v36, v36
	v_cvt_pk_bf16_f32 v10, v71, v72
	v_add_f32_e32 v9, v35, v38
	v_and_b32_e32 v31, 0xffff0000, v10
	v_lshlrev_b32_e32 v15, 16, v10
	v_mul_f32_e32 v11, v31, v31
	v_fmac_f32_e32 v11, v15, v15
	v_add_f32_e32 v9, v9, v11
; #define GAS __attribute__((address_space(1)))
; __device__ __forceinline__ unsigned pk2(float lo, float hi) { unsigned r; asm volatile("v_cvt_pk_bf16_f32 %0, %1, %2" : "=v"(r) : "v"(lo), "v"(hi)); return r; }
; __device__ __forceinline__ unsigned pk4_fp8(float a, float b, float c, float d) { unsigned w = 0u; w = __builtin_amdgcn_cvt_pk_fp8_f32(a, b, w, false); w = __builtin_amdgcn_cvt_pk_fp8_f32(c, d, w, true); return w; }
; #define DPP_F(v, ctrl) __builtin_bit_cast(float, __builtin_amdgcn_mov_dpp(__builtin_bit_cast(int, (v)), (ctrl), 0xF, 0xF, true))
; __device__ __forceinline__ float xsum16(float v) { float a = v, b = v; PL_SWAP16(a, b); return a + b; }
; __device__ __forceinline__ float xsum32(float v) { float a = v, b = v; PL_SWAP32(a, b); return a + b; }
; __device__ __forceinline__ float wave_sum(float v) {
;     v += DPP_F(v, 0xB1); v += DPP_F(v, 0x4E); v += DPP_F(v, 0x141); v += DPP_F(v, 0x140);
;     return xsum32(xsum16(v));
; template <bool FINAL, bool ADDY = true>
; __device__ __forceinline__ void combine_phase(Frame& F, float* ssq_out) {
;     ...
;             for (int j = 0; j < 4; ++j) { u32x4 w;
; #pragma unroll
;                 for (int q = 0; q < 4; ++q) { w[q] = pk2(v[j][2 * q], v[j][2 * q + 1]); const float lo = bf_lo(w[q]), hi = bf_hi(w[q]); s += lo * lo + hi * hi; }
;                 ((GAS u32x4*)(HB + (size_t)m * DM) + F.lane)[64 * j] = w;
;                 u32x2 w8; w8.x = pk4_fp8(bf_lo(w.x), bf_hi(w.x), bf_lo(w.y), bf_hi(w.y)); w8.y = pk4_fp8(bf_lo(w.z), bf_hi(w.z), bf_lo(w.w), bf_hi(w.w));
;                 ((GAS u32x2*)(F.ws + WS_HB8 + (size_t)m * DM) + F.lane)[64 * j] = w8; }
;             s = wave_sum(s); if (F.lane == 0) ssq_out[m] = s;
	v_cvt_pk_bf16_f32 v11, v73, v74
	v_mov_b32_e32 v14, 0
	v_and_b32_e32 v33, 0xffff0000, v11
	v_lshlrev_b32_e32 v32, 16, v11
	v_mul_f32_e32 v12, v33, v33
	v_fmac_f32_e32 v12, v32, v32
	v_add_f32_e32 v9, v9, v12
	v_cvt_pk_bf16_f32 v12, v75, v76
	v_cvt_pk_fp8_f32 v14, v15, v31
	v_lshlrev_b32_e32 v34, 16, v12
	v_and_b32_e32 v35, 0xffff0000, v12
	v_mov_b32_e32 v15, 0
	v_cvt_pk_fp8_f32 v15, v34, v35
	v_mul_f32_e32 v13, v35, v35
	v_fmac_f32_e32 v13, v34, v34
	v_add_f32_e32 v9, v9, v13
	v_cvt_pk_bf16_f32 v13, v77, v78
	v_cvt_pk_fp8_f32 v14, v32, v33 op_sel:[0,0,1]
	v_lshlrev_b32_e32 v36, 16, v13
	v_and_b32_e32 v31, 0xffff0000, v13
	v_cvt_pk_fp8_f32 v15, v36, v31 op_sel:[0,0,1]
	v_mul_f32_e32 v34, v31, v31
	global_store_dwordx4 v[4:5], v[10:13], off offset:1024
	global_store_dwordx2 v[6:7], v[14:15], off offset:512
	s_nop 0
	v_cvt_pk_bf16_f32 v10, v79, v16
	v_fmac_f32_e32 v34, v36, v36
	v_and_b32_e32 v16, 0xffff0000, v10
	v_lshlrev_b32_e32 v15, 16, v10
	v_mul_f32_e32 v11, v16, v16
	v_add_f32_e32 v9, v9, v34
	v_fmac_f32_e32 v11, v15, v15
	v_add_f32_e32 v9, v9, v11
	v_cvt_pk_bf16_f32 v11, v17, v18
	v_mov_b32_e32 v14, 0
	v_and_b32_e32 v18, 0xffff0000, v11
	v_lshlrev_b32_e32 v17, 16, v11
	v_mul_f32_e32 v12, v18, v18
	v_fmac_f32_e32 v12, v17, v17
	v_add_f32_e32 v9, v9, v12
	v_cvt_pk_bf16_f32 v12, v19, v20
	v_cvt_pk_fp8_f32 v14, v15, v16
	v_lshlrev_b32_e32 v19, 16, v12
	v_and_b32_e32 v20, 0xffff0000, v12
	v_mov_b32_e32 v15, 0
	v_cvt_pk_fp8_f32 v15, v19, v20
	v_mul_f32_e32 v13, v20, v20
	v_fmac_f32_e32 v13, v19, v19
	v_add_f32_e32 v9, v9, v13
	v_cvt_pk_bf16_f32 v13, v26, v21
	v_cvt_pk_fp8_f32 v14, v17, v18 op_sel:[0,0,1]
	v_lshlrev_b32_e32 v21, 16, v13
	v_and_b32_e32 v16, 0xffff0000, v13
	v_cvt_pk_fp8_f32 v15, v21, v16 op_sel:[0,0,1]
	v_mul_f32_e32 v19, v16, v16
	global_store_dwordx4 v[4:5], v[10:13], off offset:2048
	global_store_dwordx2 v[6:7], v[14:15], off offset:1024
	s_nop 0
	v_cvt_pk_bf16_f32 v10, v27, v22
	v_fmac_f32_e32 v19, v21, v21
	v_and_b32_e32 v16, 0xffff0000, v10
	v_lshlrev_b32_e32 v15, 16, v10
	v_mul_f32_e32 v11, v16, v16
	v_add_f32_e32 v9, v9, v19
	v_fmac_f32_e32 v11, v15, v15
	v_add_f32_e32 v9, v9, v11
	v_cvt_pk_bf16_f32 v11, v28, v23
	v_mov_b32_e32 v14, 0
	v_and_b32_e32 v18, 0xffff0000, v11
	v_lshlrev_b32_e32 v17, 16, v11
	v_mul_f32_e32 v12, v18, v18
	v_fmac_f32_e32 v12, v17, v17
	v_add_f32_e32 v9, v9, v12
	v_cvt_pk_bf16_f32 v12, v29, v24
	v_cvt_pk_fp8_f32 v14, v15, v16
	v_lshlrev_b32_e32 v19, 16, v12
	v_and_b32_e32 v20, 0xffff0000, v12
	v_mov_b32_e32 v15, 0
	v_cvt_pk_fp8_f32 v15, v19, v20
	v_mul_f32_e32 v13, v20, v20
	v_fmac_f32_e32 v13, v19, v19
	v_add_f32_e32 v9, v9, v13
	v_cvt_pk_bf16_f32 v13, v30, v25
	v_cvt_pk_fp8_f32 v14, v17, v18 op_sel:[0,0,1]
	v_lshlrev_b32_e32 v21, 16, v13
	v_and_b32_e32 v16, 0xffff0000, v13
	v_mul_f32_e32 v19, v16, v16
	v_cvt_pk_fp8_f32 v15, v21, v16 op_sel:[0,0,1]
	v_fmac_f32_e32 v19, v21, v21
	v_add_f32_e32 v9, v9, v19
	global_store_dwordx4 v[4:5], v[10:13], off offset:3072
	global_store_dwordx2 v[6:7], v[14:15], off offset:1536
	v_add_f32_dpp v4, v9, v9 quad_perm:[1,0,3,2] row_mask:0xf bank_mask:0xf bound_ctrl:1
	s_nop 1
	v_add_f32_dpp v4, v4, v4 quad_perm:[2,3,0,1] row_mask:0xf bank_mask:0xf bound_ctrl:1
	s_nop 1
	v_add_f32_dpp v4, v4, v4 row_half_mirror row_mask:0xf bank_mask:0xf bound_ctrl:1
	s_nop 1
	v_add_f32_dpp v4, v4, v4 row_mirror row_mask:0xf bank_mask:0xf bound_ctrl:1
	v_mov_b32_e32 v5, v4
	s_nop 1
	v_permlane16_swap_b32 v4, v5
	s_nop 0
	v_add_f32_e32 v4, v4, v5
	v_mov_b32_e32 v5, v4
	s_nop 1
	v_permlane32_swap_b32 v4, v5
	s_and_saveexec_b64 s[16:17], s[2:3]
	s_add_u32 s22, s28, s98
	v_add_f32_e32 v4, v4, v5
	s_addc_u32 s23, s29, s99
	global_store_dword v8, v4, s[22:23]
	s_or_b64 exec, exec, s[16:17]
	s_sub_i32 s16, s6, s8
	s_cmp_lt_i32 s16, 0x8000
	s_cbranch_scc0 .LBB0_887
	v_lshl_add_u64 v[4:5], s[28:29], 0, v[0:1]
	v_lshl_add_u64 v[26:27], s[28:29], 0, v[2:3]
	v_add_co_u32_e32 v4, vcc, 0x12000000, v4
	s_nop 1
	v_addc_co_u32_e32 v5, vcc, 0, v5, vcc
	v_add_co_u32_e32 v32, vcc, 0x1e800000, v26
	s_nop 1
	v_addc_co_u32_e32 v33, vcc, 0, v27, vcc
	global_load_dwordx4 v[10:13], v[4:5], off
	global_load_dwordx4 v[14:17], v[4:5], off offset:1024
	global_load_dwordx4 v[18:21], v[4:5], off offset:2048
	global_load_dwordx4 v[22:25], v[4:5], off offset:3072
	global_load_dwordx2 v[28:29], v[32:33], off
	global_load_dwordx2 v[30:31], v[32:33], off offset:512
	global_load_dwordx2 v[34:35], v[32:33], off offset:1024
	global_load_dwordx2 v[42:43], v[32:33], off offset:1536
	v_add_co_u32_e32 v32, vcc, 0x22800000, v26
	s_nop 1
	v_addc_co_u32_e32 v33, vcc, 0, v27, vcc
	global_load_dwordx2 v[36:37], v[32:33], off
	global_load_dwordx2 v[38:39], v[32:33], off offset:512
	global_load_dwordx2 v[40:41], v[32:33], off offset:1024
	global_load_dwordx2 v[44:45], v[32:33], off offset:1536
	v_add_co_u32_e32 v6, vcc, s7, v26
	s_nop 1
	v_addc_co_u32_e32 v7, vcc, 0, v27, vcc
	s_mov_b64 s[98:99], s[18:19]
	s_add_i32 s6, s6, s8
	s_cmp_lt_i32 s6, 0x8000
	s_cbranch_scc0 .Lp7_noadv_A1
	s_add_u32 s18, s18, s10
	s_addc_u32 s19, s19, s11
	v_lshl_add_u64 v[2:3], v[2:3], 0, s[12:13]
	v_lshl_add_u64 v[0:1], v[0:1], 0, s[14:15]
; #define GAS __attribute__((address_space(1)))
; __device__ __forceinline__ unsigned pk2(float lo, float hi) { unsigned r; asm volatile("v_cvt_pk_bf16_f32 %0, %1, %2" : "=v"(r) : "v"(lo), "v"(hi)); return r; }
; __device__ __forceinline__ unsigned pk4_fp8(float a, float b, float c, float d) { unsigned w = 0u; w = __builtin_amdgcn_cvt_pk_fp8_f32(a, b, w, false); w = __builtin_amdgcn_cvt_pk_fp8_f32(c, d, w, true); return w; }
; template <bool FINAL, bool ADDY = true>
; __device__ __forceinline__ void combine_phase(Frame& F, float* ssq_out) {
;     ...
;         const GAS u32x4* h4 = (const GAS u32x4*)(HB + (size_t)m * DM) + F.lane; const GAS u32x2* a4 = (const GAS u32x2*)(Y0 + (size_t)m * DM) + F.lane; const GAS u32x2* b4 = (const GAS u32x2*)(Y1 + (size_t)m * DM) + F.lane;
;         float v[4][8]; float s = 0.f;
; #pragma unroll
;         for (int j = 0; j < 4; ++j) { const u32x4 h = h4[64 * j]; u32x2 a = {0u, 0u}, b = {0u, 0u}; if (ADDY) { a = a4[64 * j]; b = b4[64 * j]; }
; #pragma unroll
;             for (int q = 0; q < 4; ++q) { const unsigned aw = q < 2 ? a.x : a.y, bw = q < 2 ? b.x : b.y;
;                 const f32x2 ya = (q & 1) ? __builtin_amdgcn_cvt_pk_f32_fp8((int)aw, true) : __builtin_amdgcn_cvt_pk_f32_fp8((int)aw, false), yb = (q & 1) ? __builtin_amdgcn_cvt_pk_f32_fp8((int)bw, true) : __builtin_amdgcn_cvt_pk_f32_fp8((int)bw, false);
;                 v[j][2 * q] = bf_lo(h[q]) + (ADDY ? (ya.x + yb.x) * (1.f / WD_SCALE) : 0.f); v[j][2 * q + 1] = bf_hi(h[q]) + (ADDY ? (ya.y + yb.y) * (1.f / WD_SCALE) : 0.f); } }
;         if constexpr (!FINAL) {
; #pragma unroll
;             for (int j = 0; j < 4; ++j) { u32x4 w;
; #pragma unroll
;                 for (int q = 0; q < 4; ++q) { w[q] = pk2(v[j][2 * q], v[j][2 * q + 1]); const float lo = bf_lo(w[q]), hi = bf_hi(w[q]); s += lo * lo + hi * hi; }
;                 ((GAS u32x4*)(HB + (size_t)m * DM) + F.lane)[64 * j] = w;
;                 u32x2 w8; w8.x = pk4_fp8(bf_lo(w.x), bf_hi(w.x), bf_lo(w.y), bf_hi(w.y)); w8.y = pk4_fp8(bf_lo(w.z), bf_hi(w.z), bf_lo(w.w), bf_hi(w.w));
;                 ((GAS u32x2*)(F.ws + WS_HB8 + (size_t)m * DM) + F.lane)[64 * j] = w8; }
.Lp7_noadv_A1:
	s_waitcnt vmcnt(21)
	v_lshlrev_b32_e32 v9, 16, v120
	v_and_b32_e32 v64, 0xffff0000, v120
	v_lshlrev_b32_e32 v65, 16, v121
	v_and_b32_e32 v66, 0xffff0000, v121
	v_cvt_pk_f32_fp8_e32 v[120:121], v136
	v_cvt_pk_f32_fp8_e32 v[50:51], v142
	v_lshlrev_b32_e32 v67, 16, v122
	v_and_b32_e32 v68, 0xffff0000, v122
	v_lshlrev_b32_e32 v69, 16, v123
	v_and_b32_e32 v70, 0xffff0000, v123
	v_lshlrev_b32_e32 v71, 16, v124
	v_and_b32_e32 v72, 0xffff0000, v124
	v_lshlrev_b32_e32 v73, 16, v125
	v_and_b32_e32 v74, 0xffff0000, v125
	v_cvt_pk_f32_fp8_sdwa v[122:123], v136 src0_sel:WORD_1
	v_cvt_pk_f32_fp8_e32 v[124:125], v137
	v_cvt_pk_f32_fp8_sdwa v[52:53], v142 src0_sel:WORD_1
	v_cvt_pk_f32_fp8_e32 v[54:55], v143
	v_lshlrev_b32_e32 v75, 16, v126
	v_and_b32_e32 v76, 0xffff0000, v126
	v_lshlrev_b32_e32 v77, 16, v127
	v_and_b32_e32 v78, 0xffff0000, v127
	v_cvt_pk_f32_fp8_sdwa v[126:127], v137 src0_sel:WORD_1
	v_cvt_pk_f32_fp8_sdwa v[142:143], v143 src0_sel:WORD_1
	v_pk_add_f32 v[120:121], v[120:121], v[50:51]
	v_cvt_pk_f32_fp8_sdwa v[48:49], v140 src0_sel:WORD_1
	v_pk_add_f32 v[122:123], v[122:123], v[52:53]
	v_pk_add_f32 v[124:125], v[124:125], v[54:55]
	v_fmac_f32_e32 v9, 0x3d800000, v120
	v_fmac_f32_e32 v64, 0x3d800000, v121
	v_cvt_pk_f32_fp8_sdwa v[120:121], v146 src0_sel:WORD_1
	v_fmac_f32_e32 v65, 0x3d800000, v122
	v_fmac_f32_e32 v66, 0x3d800000, v123
	v_fmac_f32_e32 v67, 0x3d800000, v124
	v_fmac_f32_e32 v68, 0x3d800000, v125
	v_cvt_pk_f32_fp8_e32 v[122:123], v141
	v_cvt_pk_f32_fp8_e32 v[124:125], v147
	v_pk_add_f32 v[126:127], v[126:127], v[142:143]
	v_lshlrev_b32_e32 v79, 16, v128
	v_fmac_f32_e32 v69, 0x3d800000, v126
	v_fmac_f32_e32 v70, 0x3d800000, v127
	v_and_b32_e32 v126, 0xffff0000, v128
	v_lshlrev_b32_e32 v127, 16, v129
	v_pk_add_f32 v[120:121], v[48:49], v[120:121]
	v_and_b32_e32 v128, 0xffff0000, v129
	v_fmac_f32_e32 v127, 0x3d800000, v120
	v_fmac_f32_e32 v128, 0x3d800000, v121
	v_pk_add_f32 v[120:121], v[122:123], v[124:125]
	v_cvt_pk_f32_fp8_sdwa v[122:123], v141 src0_sel:WORD_1
	v_cvt_pk_f32_fp8_sdwa v[124:125], v147 src0_sel:WORD_1
	v_cvt_pk_f32_fp8_e32 v[26:27], v138
	v_cvt_pk_f32_fp8_e32 v[56:57], v144
	v_lshlrev_b32_e32 v129, 16, v130
	v_and_b32_e32 v130, 0xffff0000, v130
	v_fmac_f32_e32 v129, 0x3d800000, v120
	v_fmac_f32_e32 v130, 0x3d800000, v121
	v_pk_add_f32 v[120:121], v[122:123], v[124:125]
	v_cvt_pk_f32_fp8_e32 v[122:123], v148
	v_cvt_pk_f32_fp8_e32 v[124:125], v150
	v_pk_add_f32 v[26:27], v[26:27], v[56:57]
	v_cvt_pk_f32_fp8_sdwa v[136:137], v138 src0_sel:WORD_1
	v_fmac_f32_e32 v71, 0x3d800000, v26
	v_lshlrev_b32_e32 v26, 16, v131
	v_and_b32_e32 v131, 0xffff0000, v131
	v_fmac_f32_e32 v26, 0x3d800000, v120
	v_fmac_f32_e32 v131, 0x3d800000, v121
	v_pk_add_f32 v[120:121], v[122:123], v[124:125]
	v_cvt_pk_f32_fp8_sdwa v[122:123], v148 src0_sel:WORD_1
	v_cvt_pk_f32_fp8_sdwa v[124:125], v150 src0_sel:WORD_1
	v_cvt_pk_f32_fp8_sdwa v[58:59], v144 src0_sel:WORD_1
	v_fmac_f32_e32 v72, 0x3d800000, v27
	v_lshlrev_b32_e32 v27, 16, v132
	v_and_b32_e32 v132, 0xffff0000, v132
	v_fmac_f32_e32 v27, 0x3d800000, v120
	v_fmac_f32_e32 v132, 0x3d800000, v121
	v_pk_add_f32 v[120:121], v[122:123], v[124:125]
	v_cvt_pk_f32_fp8_e32 v[122:123], v149
	v_cvt_pk_f32_fp8_e32 v[124:125], v151
	v_pk_add_f32 v[136:137], v[136:137], v[58:59]
	v_cvt_pk_f32_fp8_e32 v[32:33], v139
	v_cvt_pk_f32_fp8_sdwa v[138:139], v139 src0_sel:WORD_1
	v_cvt_pk_f32_fp8_e32 v[60:61], v145
	v_cvt_pk_f32_fp8_sdwa v[144:145], v145 src0_sel:WORD_1
	v_fmac_f32_e32 v73, 0x3d800000, v136
	v_lshlrev_b32_e32 v136, 16, v133
	v_and_b32_e32 v133, 0xffff0000, v133
	v_fmac_f32_e32 v136, 0x3d800000, v120
	v_fmac_f32_e32 v133, 0x3d800000, v121
	v_pk_add_f32 v[120:121], v[122:123], v[124:125]
	v_cvt_pk_f32_fp8_sdwa v[122:123], v149 src0_sel:WORD_1
	v_cvt_pk_f32_fp8_sdwa v[124:125], v151 src0_sel:WORD_1
	v_pk_add_f32 v[138:139], v[138:139], v[144:145]
	v_fmac_f32_e32 v74, 0x3d800000, v137
	v_lshlrev_b32_e32 v137, 16, v134
	v_and_b32_e32 v134, 0xffff0000, v134
	v_pk_add_f32 v[32:33], v[32:33], v[60:61]
	v_fmac_f32_e32 v77, 0x3d800000, v138
	v_fmac_f32_e32 v137, 0x3d800000, v120
	v_fmac_f32_e32 v134, 0x3d800000, v121
	v_lshlrev_b32_e32 v138, 16, v135
	v_pk_add_f32 v[120:121], v[122:123], v[124:125]
	v_and_b32_e32 v135, 0xffff0000, v135
	v_fmac_f32_e32 v75, 0x3d800000, v32
	v_fmac_f32_e32 v138, 0x3d800000, v120
	v_fmac_f32_e32 v135, 0x3d800000, v121
	v_cvt_pk_bf16_f32 v120, v9, v64
	v_cvt_pk_bf16_f32 v121, v65, v66
	v_fmac_f32_e32 v78, 0x3d800000, v139
	v_and_b32_e32 v125, 0xffff0000, v120
	v_and_b32_e32 v32, 0xffff0000, v121
	v_lshlrev_b32_e32 v9, 16, v120
	v_mul_f32_e32 v122, v125, v125
	v_lshlrev_b32_e32 v139, 16, v121
	v_mul_f32_e32 v123, v32, v32
	v_fmac_f32_e32 v122, v9, v9
	v_fmac_f32_e32 v123, v139, v139
	v_cvt_pk_f32_fp8_e32 v[46:47], v140
	v_add_f32_e32 v123, v122, v123
	v_cvt_pk_bf16_f32 v122, v67, v68
	v_fmac_f32_e32 v76, 0x3d800000, v33
	v_and_b32_e32 v140, 0xffff0000, v122
	v_lshlrev_b32_e32 v33, 16, v122
	v_mul_f32_e32 v124, v140, v140
; #define GAS __attribute__((address_space(1)))
; __device__ __forceinline__ unsigned pk2(float lo, float hi) { unsigned r; asm volatile("v_cvt_pk_bf16_f32 %0, %1, %2" : "=v"(r) : "v"(lo), "v"(hi)); return r; }
; __device__ __forceinline__ unsigned pk4_fp8(float a, float b, float c, float d) { unsigned w = 0u; w = __builtin_amdgcn_cvt_pk_fp8_f32(a, b, w, false); w = __builtin_amdgcn_cvt_pk_fp8_f32(c, d, w, true); return w; }
; #define DPP_F(v, ctrl) __builtin_bit_cast(float, __builtin_amdgcn_mov_dpp(__builtin_bit_cast(int, (v)), (ctrl), 0xF, 0xF, true))
; __device__ __forceinline__ float xsum16(float v) { float a = v, b = v; PL_SWAP16(a, b); return a + b; }
; __device__ __forceinline__ float xsum32(float v) { float a = v, b = v; PL_SWAP32(a, b); return a + b; }
; __device__ __forceinline__ float wave_sum(float v) {
;     v += DPP_F(v, 0xB1); v += DPP_F(v, 0x4E); v += DPP_F(v, 0x141); v += DPP_F(v, 0x140);
;     return xsum32(xsum16(v));
; template <bool FINAL, bool ADDY = true>
; __device__ __forceinline__ void combine_phase(Frame& F, float* ssq_out) {
;     ...
;             for (int j = 0; j < 4; ++j) { u32x4 w;
; #pragma unroll
;                 for (int q = 0; q < 4; ++q) { w[q] = pk2(v[j][2 * q], v[j][2 * q + 1]); const float lo = bf_lo(w[q]), hi = bf_hi(w[q]); s += lo * lo + hi * hi; }
;                 ((GAS u32x4*)(HB + (size_t)m * DM) + F.lane)[64 * j] = w;
;                 u32x2 w8; w8.x = pk4_fp8(bf_lo(w.x), bf_hi(w.x), bf_lo(w.y), bf_hi(w.y)); w8.y = pk4_fp8(bf_lo(w.z), bf_hi(w.z), bf_lo(w.w), bf_hi(w.w));
;                 ((GAS u32x2*)(F.ws + WS_HB8 + (size_t)m * DM) + F.lane)[64 * j] = w8; }
;             s = wave_sum(s); if (F.lane == 0) ssq_out[m] = s;
	v_fmac_f32_e32 v124, v33, v33
	v_cvt_pk_f32_fp8_e32 v[62:63], v146
	v_add_f32_e32 v141, v123, v124
	v_mov_b32_e32 v124, 0
	v_cvt_pk_fp8_f32 v124, v9, v125
	v_mov_b32_e32 v125, 0
	v_cvt_pk_fp8_f32 v125, v33, v140
	v_pk_add_f32 v[142:143], v[46:47], v[62:63]
	v_cvt_pk_bf16_f32 v123, v69, v70
	v_cvt_pk_fp8_f32 v124, v139, v32 op_sel:[0,0,1]
	v_fmac_f32_e32 v79, 0x3d800000, v142
	v_fmac_f32_e32 v126, 0x3d800000, v143
	v_lshlrev_b32_e32 v142, 16, v123
	v_and_b32_e32 v143, 0xffff0000, v123
	v_cvt_pk_fp8_f32 v125, v142, v143 op_sel:[0,0,1]
	v_mul_f32_e32 v144, v143, v143
	global_store_dwordx4 v[116:117], v[120:123], off
	global_store_dwordx2 v[118:119], v[124:125], off
	v_fmac_f32_e32 v144, v142, v142
	v_cvt_pk_bf16_f32 v120, v71, v72
	v_add_f32_e32 v9, v141, v144
	v_and_b32_e32 v139, 0xffff0000, v120
	v_lshlrev_b32_e32 v125, 16, v120
	v_mul_f32_e32 v121, v139, v139
	v_fmac_f32_e32 v121, v125, v125
	v_add_f32_e32 v9, v9, v121
	v_cvt_pk_bf16_f32 v121, v73, v74
	v_mov_b32_e32 v124, 0
	v_and_b32_e32 v33, 0xffff0000, v121
	v_lshlrev_b32_e32 v32, 16, v121
	v_mul_f32_e32 v122, v33, v33
	v_fmac_f32_e32 v122, v32, v32
	v_add_f32_e32 v9, v9, v122
	v_cvt_pk_bf16_f32 v122, v75, v76
	v_cvt_pk_fp8_f32 v124, v125, v139
	v_lshlrev_b32_e32 v140, 16, v122
	v_and_b32_e32 v141, 0xffff0000, v122
	v_mov_b32_e32 v125, 0
	v_cvt_pk_fp8_f32 v125, v140, v141
	v_mul_f32_e32 v123, v141, v141
	v_fmac_f32_e32 v123, v140, v140
	v_add_f32_e32 v9, v9, v123
	v_cvt_pk_bf16_f32 v123, v77, v78
	v_cvt_pk_fp8_f32 v124, v32, v33 op_sel:[0,0,1]
	v_lshlrev_b32_e32 v142, 16, v123
	v_and_b32_e32 v139, 0xffff0000, v123
	v_cvt_pk_fp8_f32 v125, v142, v139 op_sel:[0,0,1]
	v_mul_f32_e32 v140, v139, v139
	global_store_dwordx4 v[116:117], v[120:123], off offset:1024
	global_store_dwordx2 v[118:119], v[124:125], off offset:512
	s_nop 0
	v_cvt_pk_bf16_f32 v120, v79, v126
	v_fmac_f32_e32 v140, v142, v142
	v_and_b32_e32 v126, 0xffff0000, v120
	v_lshlrev_b32_e32 v125, 16, v120
	v_mul_f32_e32 v121, v126, v126
	v_add_f32_e32 v9, v9, v140
	v_fmac_f32_e32 v121, v125, v125
	v_add_f32_e32 v9, v9, v121
	v_cvt_pk_bf16_f32 v121, v127, v128
	v_mov_b32_e32 v124, 0
	v_and_b32_e32 v128, 0xffff0000, v121
	v_lshlrev_b32_e32 v127, 16, v121
	v_mul_f32_e32 v122, v128, v128
	v_fmac_f32_e32 v122, v127, v127
	v_add_f32_e32 v9, v9, v122
	v_cvt_pk_bf16_f32 v122, v129, v130
	v_cvt_pk_fp8_f32 v124, v125, v126
	v_lshlrev_b32_e32 v129, 16, v122
	v_and_b32_e32 v130, 0xffff0000, v122
	v_mov_b32_e32 v125, 0
	v_cvt_pk_fp8_f32 v125, v129, v130
	v_mul_f32_e32 v123, v130, v130
	v_fmac_f32_e32 v123, v129, v129
	v_add_f32_e32 v9, v9, v123
	v_cvt_pk_bf16_f32 v123, v26, v131
	v_cvt_pk_fp8_f32 v124, v127, v128 op_sel:[0,0,1]
	v_lshlrev_b32_e32 v131, 16, v123
	v_and_b32_e32 v126, 0xffff0000, v123
	v_cvt_pk_fp8_f32 v125, v131, v126 op_sel:[0,0,1]
	v_mul_f32_e32 v129, v126, v126
	global_store_dwordx4 v[116:117], v[120:123], off offset:2048
	global_store_dwordx2 v[118:119], v[124:125], off offset:1024
	s_nop 0
	v_cvt_pk_bf16_f32 v120, v27, v132
	v_fmac_f32_e32 v129, v131, v131
	v_and_b32_e32 v126, 0xffff0000, v120
	v_lshlrev_b32_e32 v125, 16, v120
	v_mul_f32_e32 v121, v126, v126
	v_add_f32_e32 v9, v9, v129
	v_fmac_f32_e32 v121, v125, v125
	v_add_f32_e32 v9, v9, v121
	v_cvt_pk_bf16_f32 v121, v136, v133
	v_mov_b32_e32 v124, 0
	v_and_b32_e32 v128, 0xffff0000, v121
	v_lshlrev_b32_e32 v127, 16, v121
	v_mul_f32_e32 v122, v128, v128
	v_fmac_f32_e32 v122, v127, v127
	v_add_f32_e32 v9, v9, v122
	v_cvt_pk_bf16_f32 v122, v137, v134
	v_cvt_pk_fp8_f32 v124, v125, v126
	v_lshlrev_b32_e32 v129, 16, v122
	v_and_b32_e32 v130, 0xffff0000, v122
	v_mov_b32_e32 v125, 0
	v_cvt_pk_fp8_f32 v125, v129, v130
	v_mul_f32_e32 v123, v130, v130
	v_fmac_f32_e32 v123, v129, v129
	v_add_f32_e32 v9, v9, v123
	v_cvt_pk_bf16_f32 v123, v138, v135
	v_cvt_pk_fp8_f32 v124, v127, v128 op_sel:[0,0,1]
	v_lshlrev_b32_e32 v131, 16, v123
	v_and_b32_e32 v126, 0xffff0000, v123
	v_mul_f32_e32 v129, v126, v126
	v_cvt_pk_fp8_f32 v125, v131, v126 op_sel:[0,0,1]
	v_fmac_f32_e32 v129, v131, v131
	v_add_f32_e32 v9, v9, v129
	global_store_dwordx4 v[116:117], v[120:123], off offset:3072
	global_store_dwordx2 v[118:119], v[124:125], off offset:1536
	v_add_f32_dpp v116, v9, v9 quad_perm:[1,0,3,2] row_mask:0xf bank_mask:0xf bound_ctrl:1
	s_nop 1
	v_add_f32_dpp v116, v116, v116 quad_perm:[2,3,0,1] row_mask:0xf bank_mask:0xf bound_ctrl:1
	s_nop 1
	v_add_f32_dpp v116, v116, v116 row_half_mirror row_mask:0xf bank_mask:0xf bound_ctrl:1
	s_nop 1
	v_add_f32_dpp v116, v116, v116 row_mirror row_mask:0xf bank_mask:0xf bound_ctrl:1
	v_mov_b32_e32 v117, v116
	s_nop 1
	v_permlane16_swap_b32 v116, v117
	s_nop 0
	v_add_f32_e32 v116, v116, v117
	v_mov_b32_e32 v117, v116
	s_nop 1
	v_permlane32_swap_b32 v116, v117
	s_and_saveexec_b64 s[16:17], s[2:3]
	s_add_u32 s22, s28, s100
	v_add_f32_e32 v116, v116, v117
	s_addc_u32 s23, s29, s101
	global_store_dword v8, v116, s[22:23]
	s_or_b64 exec, exec, s[16:17]
	s_sub_i32 s16, s6, s8
	s_cmp_lt_i32 s16, 0x8000
	s_cbranch_scc0 .LBB0_887
	s_branch .Lp7_loop
